# grid barrier non-leader path: agent-scope L1 invalidate issued before polling the release word (waves are parked, only sc1 polls run in between) instead of after it
# speedup vs baseline: 1.0070x; 1.0070x over previous
.LBB0_171:
	s_or_b64 exec, exec, s[8:9]
	v_cvt_f32_u32_e32 v4, v2
	s_waitcnt vmcnt(0)
	v_readfirstlane_b32 s4, v3
	v_sub_u32_e32 v3, 0, v2
	v_rcp_iflag_f32_e32 v4, v4
	v_add_u32_e32 v5, s4, v1
	v_mul_f32_e32 v4, 0x4f7ffffe, v4
	v_cvt_u32_f32_e32 v4, v4
	v_mul_lo_u32 v1, v3, v4
	v_mul_hi_u32 v1, v4, v1
	v_add_u32_e32 v1, v4, v1
	v_mul_hi_u32 v1, v5, v1
	v_mul_lo_u32 v3, v1, v2
	v_sub_u32_e32 v3, v5, v3
	v_add_u32_e32 v4, 1, v1
	v_cmp_ge_u32_e32 vcc, v3, v2
	s_nop 1
	v_cndmask_b32_e32 v1, v1, v4, vcc
	v_sub_u32_e32 v4, v3, v2
	v_cndmask_b32_e32 v3, v3, v4, vcc
	v_add_u32_e32 v4, 1, v1
	v_cmp_ge_u32_e32 vcc, v3, v2
	v_add_u32_e32 v3, 1, v5
	s_nop 0
	v_cndmask_b32_e32 v1, v1, v4, vcc
	v_mul_lo_u32 v4, v2, v1
	v_add_u32_e32 v2, v4, v2
	v_cmp_ne_u32_e32 vcc, v3, v2
	s_and_saveexec_b64 s[4:5], vcc
	s_xor_b64 s[6:7], exec, s[4:5]
	s_cbranch_execz .LBB0_185
	buffer_inv sc1
	s_waitcnt lgkmcnt(0)
	v_mov_b32_e32 v0, 0x2000
	global_load_dword v0, v0, s[2:3] offset:1024 sc1
	s_add_u32 s12, s2, 0x2400
	s_addc_u32 s13, s3, 0
	s_waitcnt vmcnt(0)
	v_cmp_eq_u32_e32 vcc, v0, v1
	s_and_saveexec_b64 s[8:9], vcc
	s_cbranch_execz .LBB0_184
	s_add_u32 s10, s46, 0x4200
	s_addc_u32 s11, s47, 0
	s_mov_b32 s4, 1
	s_mov_b64 s[14:15], 0
	v_mov_b32_e32 v0, 0
	s_branch .LBB0_175

.LBB0_184:
	s_or_b64 exec, exec, s[8:9]
	s_waitcnt vmcnt(0)
	s_waitcnt vmcnt(0)

.LBB0_289:
	s_or_b64 exec, exec, s[6:7]
	v_cvt_f32_u32_e32 v5, v3
	s_waitcnt vmcnt(0)
	v_readfirstlane_b32 s4, v4
	v_sub_u32_e32 v4, 0, v3
	v_rcp_iflag_f32_e32 v5, v5
	v_add_u32_e32 v6, s4, v0
	v_mul_f32_e32 v5, 0x4f7ffffe, v5
	v_cvt_u32_f32_e32 v5, v5
	v_mul_lo_u32 v0, v4, v5
	v_mul_hi_u32 v0, v5, v0
	v_add_u32_e32 v0, v5, v0
	v_mul_hi_u32 v0, v6, v0
	v_mul_lo_u32 v4, v0, v3
	v_sub_u32_e32 v4, v6, v4
	v_add_u32_e32 v5, 1, v0
	v_cmp_ge_u32_e32 vcc, v4, v3
	s_nop 1
	v_cndmask_b32_e32 v0, v0, v5, vcc
	v_sub_u32_e32 v5, v4, v3
	v_cndmask_b32_e32 v4, v4, v5, vcc
	v_add_u32_e32 v5, 1, v0
	v_cmp_ge_u32_e32 vcc, v4, v3
	v_add_u32_e32 v4, 1, v6
	s_nop 0
	v_cndmask_b32_e32 v0, v0, v5, vcc
	v_mul_lo_u32 v5, v3, v0
	v_add_u32_e32 v3, v5, v3
	v_cmp_ne_u32_e32 vcc, v4, v3
	s_and_saveexec_b64 s[4:5], vcc
	s_xor_b64 s[4:5], exec, s[4:5]
	s_cbranch_execz .LBB0_303
	buffer_inv sc1
	s_add_i32 s76, s9, 0x900
	s_lshl_b64 s[6:7], s[76:77], 2
	v_readlane_b32 s10, v254, 46
	v_readlane_b32 s11, v254, 47
	s_add_u32 s14, s10, s6
	s_addc_u32 s15, s11, s7
	s_waitcnt lgkmcnt(0)
	global_load_dword v2, v1, s[14:15] sc1
	s_waitcnt vmcnt(0)
	v_cmp_eq_u32_e32 vcc, v2, v0
	s_and_saveexec_b64 s[6:7], vcc
	s_cbranch_execz .LBB0_302
	s_mov_b32 s10, 1
	s_mov_b64 s[16:17], 0
	s_branch .LBB0_293

.LBB0_302:
	s_or_b64 exec, exec, s[6:7]
	s_waitcnt vmcnt(0)
	s_waitcnt vmcnt(0)

.LBB0_628:
	s_or_b64 exec, exec, s[6:7]
	v_cvt_f32_u32_e32 v5, v3
	s_waitcnt vmcnt(0)
	v_readfirstlane_b32 s2, v4
	v_sub_u32_e32 v4, 0, v3
	v_rcp_iflag_f32_e32 v5, v5
	v_add_u32_e32 v6, s2, v0
	v_mul_f32_e32 v5, 0x4f7ffffe, v5
	v_cvt_u32_f32_e32 v5, v5
	v_mul_lo_u32 v0, v4, v5
	v_mul_hi_u32 v0, v5, v0
	v_add_u32_e32 v0, v5, v0
	v_mul_hi_u32 v0, v6, v0
	v_mul_lo_u32 v4, v0, v3
	v_sub_u32_e32 v4, v6, v4
	v_add_u32_e32 v5, 1, v0
	v_cmp_ge_u32_e32 vcc, v4, v3
	s_nop 1
	v_cndmask_b32_e32 v0, v0, v5, vcc
	v_sub_u32_e32 v5, v4, v3
	v_cndmask_b32_e32 v4, v4, v5, vcc
	v_add_u32_e32 v5, 1, v0
	v_cmp_ge_u32_e32 vcc, v4, v3
	v_add_u32_e32 v4, 1, v6
	s_nop 0
	v_cndmask_b32_e32 v0, v0, v5, vcc
	v_mul_lo_u32 v5, v3, v0
	v_add_u32_e32 v3, v5, v3
	v_cmp_ne_u32_e32 vcc, v4, v3
	s_and_saveexec_b64 s[2:3], vcc
	s_xor_b64 s[2:3], exec, s[2:3]
	s_cbranch_execz .LBB0_642
	buffer_inv sc1
	s_add_i32 s76, s8, 0x900
	s_lshl_b64 s[6:7], s[76:77], 2
	v_readlane_b32 s10, v254, 46
	v_readlane_b32 s11, v254, 47
	s_add_u32 s14, s10, s6
	s_addc_u32 s15, s11, s7
	s_waitcnt lgkmcnt(0)
	global_load_dword v2, v1, s[14:15] sc1
	s_waitcnt vmcnt(0)
	v_cmp_eq_u32_e32 vcc, v2, v0
	s_and_saveexec_b64 s[6:7], vcc
	s_cbranch_execz .LBB0_641
	s_mov_b32 s9, 1
	s_mov_b64 s[16:17], 0
	s_branch .LBB0_632

.LBB0_794:
	s_or_b64 exec, exec, s[10:11]
	v_cvt_f32_u32_e32 v5, v3
	s_waitcnt vmcnt(0)
	v_readfirstlane_b32 s6, v4
	v_sub_u32_e32 v4, 0, v3
	v_rcp_iflag_f32_e32 v5, v5
	v_add_u32_e32 v6, s6, v0
	v_mul_f32_e32 v5, 0x4f7ffffe, v5
	v_cvt_u32_f32_e32 v5, v5
	v_mul_lo_u32 v0, v4, v5
	v_mul_hi_u32 v0, v5, v0
	v_add_u32_e32 v0, v5, v0
	v_mul_hi_u32 v0, v6, v0
	v_mul_lo_u32 v4, v0, v3
	v_sub_u32_e32 v4, v6, v4
	v_add_u32_e32 v5, 1, v0
	v_cmp_ge_u32_e32 vcc, v4, v3
	s_nop 1
	v_cndmask_b32_e32 v0, v0, v5, vcc
	v_sub_u32_e32 v5, v4, v3
	v_cndmask_b32_e32 v4, v4, v5, vcc
	v_add_u32_e32 v5, 1, v0
	v_cmp_ge_u32_e32 vcc, v4, v3
	v_add_u32_e32 v4, 1, v6
	s_nop 0
	v_cndmask_b32_e32 v0, v0, v5, vcc
	v_mul_lo_u32 v5, v3, v0
	v_add_u32_e32 v3, v5, v3
	v_cmp_ne_u32_e32 vcc, v4, v3
	s_and_saveexec_b64 s[6:7], vcc
	s_xor_b64 s[6:7], exec, s[6:7]
	s_cbranch_execz .LBB0_808
	buffer_inv sc1
	s_add_i32 s76, s8, 0x900
	s_lshl_b64 s[10:11], s[76:77], 2
	v_readlane_b32 s12, v254, 46
	v_readlane_b32 s13, v254, 47
	s_add_u32 s12, s12, s10
	s_addc_u32 s13, s13, s11
	s_waitcnt lgkmcnt(0)
	s_nop 1
	global_load_dword v2, v1, s[12:13] sc1
	s_waitcnt vmcnt(0)
	v_cmp_eq_u32_e32 vcc, v2, v0
	s_and_saveexec_b64 s[10:11], vcc
	s_cbranch_execz .LBB0_807
	s_mov_b32 s9, 1
	s_mov_b64 s[14:15], 0
	s_branch .LBB0_798

.LBB0_807:
	s_or_b64 exec, exec, s[10:11]
	s_waitcnt vmcnt(0)
	s_waitcnt vmcnt(0)

.LBB0_897:
	s_or_b64 exec, exec, s[4:5]
	v_cvt_f32_u32_e32 v5, v3
	s_waitcnt vmcnt(0)
	v_readfirstlane_b32 s2, v4
	v_sub_u32_e32 v4, 0, v3
	v_rcp_iflag_f32_e32 v5, v5
	v_add_u32_e32 v6, s2, v0
	v_mul_f32_e32 v5, 0x4f7ffffe, v5
	v_cvt_u32_f32_e32 v5, v5
	v_mul_lo_u32 v0, v4, v5
	v_mul_hi_u32 v0, v5, v0
	v_add_u32_e32 v0, v5, v0
	v_mul_hi_u32 v0, v6, v0
	v_mul_lo_u32 v4, v0, v3
	v_sub_u32_e32 v4, v6, v4
	v_add_u32_e32 v5, 1, v0
	v_cmp_ge_u32_e32 vcc, v4, v3
	s_nop 1
	v_cndmask_b32_e32 v0, v0, v5, vcc
	v_sub_u32_e32 v5, v4, v3
	v_cndmask_b32_e32 v4, v4, v5, vcc
	v_add_u32_e32 v5, 1, v0
	v_cmp_ge_u32_e32 vcc, v4, v3
	v_add_u32_e32 v4, 1, v6
	s_nop 0
	v_cndmask_b32_e32 v0, v0, v5, vcc
	v_mul_lo_u32 v5, v3, v0
	v_add_u32_e32 v3, v5, v3
	v_cmp_ne_u32_e32 vcc, v4, v3
	s_and_saveexec_b64 s[2:3], vcc
	s_xor_b64 s[2:3], exec, s[2:3]
	s_cbranch_execz .LBB0_911
	buffer_inv sc1
	s_add_i32 s76, s20, 0x900
	s_lshl_b64 s[4:5], s[76:77], 2
	v_readlane_b32 s6, v254, 46
	v_readlane_b32 s7, v254, 47
	s_add_u32 s6, s6, s4
	s_addc_u32 s7, s7, s5
	s_waitcnt lgkmcnt(0)
	s_nop 1
	global_load_dword v2, v1, s[6:7] sc1
	s_waitcnt vmcnt(0)
	v_cmp_eq_u32_e32 vcc, v2, v0
	s_and_saveexec_b64 s[4:5], vcc
	s_cbranch_execz .LBB0_910
	s_mov_b32 s18, 1
	s_mov_b64 s[8:9], 0
	s_branch .LBB0_901

.LBB0_910:
	s_or_b64 exec, exec, s[4:5]
	s_waitcnt vmcnt(0)
	s_waitcnt vmcnt(0)

.LBB0_1097:
	s_or_b64 exec, exec, s[6:7]
	v_cvt_f32_u32_e32 v5, v3
	s_waitcnt vmcnt(0)
	v_readfirstlane_b32 s4, v4
	v_sub_u32_e32 v4, 0, v3
	v_rcp_iflag_f32_e32 v5, v5
	v_add_u32_e32 v6, s4, v0
	v_mul_f32_e32 v5, 0x4f7ffffe, v5
	v_cvt_u32_f32_e32 v5, v5
	v_mul_lo_u32 v0, v4, v5
	v_mul_hi_u32 v0, v5, v0
	v_add_u32_e32 v0, v5, v0
	v_mul_hi_u32 v0, v6, v0
	v_mul_lo_u32 v4, v0, v3
	v_sub_u32_e32 v4, v6, v4
	v_add_u32_e32 v5, 1, v0
	v_cmp_ge_u32_e32 vcc, v4, v3
	s_nop 1
	v_cndmask_b32_e32 v0, v0, v5, vcc
	v_sub_u32_e32 v5, v4, v3
	v_cndmask_b32_e32 v4, v4, v5, vcc
	v_add_u32_e32 v5, 1, v0
	v_cmp_ge_u32_e32 vcc, v4, v3
	v_add_u32_e32 v4, 1, v6
	s_nop 0
	v_cndmask_b32_e32 v0, v0, v5, vcc
	v_mul_lo_u32 v5, v3, v0
	v_add_u32_e32 v3, v5, v3
	v_cmp_ne_u32_e32 vcc, v4, v3
	s_and_saveexec_b64 s[4:5], vcc
	s_xor_b64 s[4:5], exec, s[4:5]
	s_cbranch_execz .LBB0_1111
	buffer_inv sc1
	s_add_i32 s76, s23, 0x900
	s_lshl_b64 s[6:7], s[76:77], 2
	v_readlane_b32 s8, v254, 46
	v_readlane_b32 s9, v254, 47
	s_add_u32 s8, s8, s6
	s_addc_u32 s9, s9, s7
	s_waitcnt lgkmcnt(0)
	s_nop 1
	global_load_dword v2, v1, s[8:9] sc1
	s_waitcnt vmcnt(0)
	v_cmp_eq_u32_e32 vcc, v2, v0
	s_and_saveexec_b64 s[6:7], vcc
	s_cbranch_execz .LBB0_1110
	s_mov_b32 s20, 1
	s_mov_b64 s[10:11], 0
	s_branch .LBB0_1101

.LBB0_1184:
	s_or_b64 exec, exec, s[6:7]
	v_cvt_f32_u32_e32 v5, v3
	s_waitcnt vmcnt(0)
	v_readfirstlane_b32 s4, v4
	v_sub_u32_e32 v4, 0, v3
	v_rcp_iflag_f32_e32 v5, v5
	v_add_u32_e32 v6, s4, v0
	v_mul_f32_e32 v5, 0x4f7ffffe, v5
	v_cvt_u32_f32_e32 v5, v5
	v_mul_lo_u32 v0, v4, v5
	v_mul_hi_u32 v0, v5, v0
	v_add_u32_e32 v0, v5, v0
	v_mul_hi_u32 v0, v6, v0
	v_mul_lo_u32 v4, v0, v3
	v_sub_u32_e32 v4, v6, v4
	v_add_u32_e32 v5, 1, v0
	v_cmp_ge_u32_e32 vcc, v4, v3
	s_nop 1
	v_cndmask_b32_e32 v0, v0, v5, vcc
	v_sub_u32_e32 v5, v4, v3
	v_cndmask_b32_e32 v4, v4, v5, vcc
	v_add_u32_e32 v5, 1, v0
	v_cmp_ge_u32_e32 vcc, v4, v3
	v_add_u32_e32 v4, 1, v6
	s_nop 0
	v_cndmask_b32_e32 v0, v0, v5, vcc
	v_mul_lo_u32 v5, v3, v0
	v_add_u32_e32 v3, v5, v3
	v_cmp_ne_u32_e32 vcc, v4, v3
	s_and_saveexec_b64 s[4:5], vcc
	s_xor_b64 s[4:5], exec, s[4:5]
	s_cbranch_execz .LBB0_1198
	buffer_inv sc1
	s_add_i32 s76, s22, 0x900
	s_lshl_b64 s[6:7], s[76:77], 2
	v_readlane_b32 s8, v254, 46
	v_readlane_b32 s9, v254, 47
	s_add_u32 s8, s8, s6
	s_addc_u32 s9, s9, s7
	s_waitcnt lgkmcnt(0)
	s_nop 1
	global_load_dword v2, v1, s[8:9] sc1
	s_waitcnt vmcnt(0)
	v_cmp_eq_u32_e32 vcc, v2, v0
	s_and_saveexec_b64 s[6:7], vcc
	s_cbranch_execz .LBB0_1197
	s_mov_b32 s20, 1
	s_mov_b64 s[10:11], 0
	s_branch .LBB0_1188
